# v16 + MoE weight conversion: first item's packed output held in registers and stored next to the second item's stores (both halves of each output line back to back)
# speedup vs baseline: 1.0091x; 1.0091x over previous
.LBB0_45:
	s_lshr_b32 s7, s11, 5
	v_cvt_f32_ubyte0_e32 v34, s7
	v_rcp_iflag_f32_e32 v34, v34
	s_mulk_i32 s12, 0xf200
	s_mulk_i32 s10, 0x7000
	s_sub_i32 s16, 0, s7
	v_mul_f32_e32 v34, 0x4f7ffffe, v34
	v_cvt_u32_f32_e32 v34, v34
	s_sub_i32 s10, s12, s10
	s_add_i32 s10, s22, s10
	s_abs_i32 s13, s10
	v_readfirstlane_b32 s17, v34
	s_mul_i32 s16, s16, s17
	s_mul_hi_u32 s16, s17, s16
	s_add_i32 s17, s17, s16
	s_mul_hi_u32 s16, s13, s17
	s_mul_i32 s17, s16, s7
	s_sub_i32 s13, s13, s17
	s_ashr_i32 s12, s10, 31
	s_add_i32 s17, s16, 1
	s_sub_i32 s18, s13, s7
	s_cmp_ge_u32 s13, s7
	s_cselect_b32 s16, s17, s16
	s_cselect_b32 s13, s18, s13
	s_add_i32 s17, s16, 1
	s_cmp_ge_u32 s13, s7
	s_cselect_b32 s13, s17, s16
	s_xor_b32 s13, s13, s12
	s_sub_i32 s12, s13, s12
	s_mul_i32 s7, s12, s7
	s_sub_i32 s7, s10, s7
	s_lshl_b32 s10, s12, 7
	s_lshl_b32 s12, s7, 5
	s_ashr_i32 s13, s12, 31
	s_lshl_b64 s[16:17], s[12:13], 2
	v_or_b32_e32 v50, s10, v94
	v_lshl_add_u64 v[32:33], v[32:33], 0, s[16:17]
	v_lshl_add_u64 v[32:33], v[32:33], 0, v[74:75]
	v_mad_i64_i32 v[34:35], s[16:17], v50, s11, 0
	v_or_b32_e32 v36, 2, v50
	v_or_b32_e32 v38, 4, v50
	v_or_b32_e32 v40, 6, v50
	v_or_b32_e32 v42, 8, v50
	v_or_b32_e32 v44, 10, v50
	v_or_b32_e32 v46, 12, v50
	v_or_b32_e32 v48, 14, v50
	v_lshl_add_u64 v[34:35], v[34:35], 2, v[32:33]
	v_mad_i64_i32 v[36:37], s[16:17], v36, s11, 0
	v_mad_i64_i32 v[38:39], s[16:17], v38, s11, 0
	v_mad_i64_i32 v[40:41], s[16:17], v40, s11, 0
	v_mad_i64_i32 v[42:43], s[16:17], v42, s11, 0
	v_mad_i64_i32 v[44:45], s[16:17], v44, s11, 0
	v_mad_i64_i32 v[46:47], s[16:17], v46, s11, 0
	v_mad_i64_i32 v[48:49], s[16:17], v48, s11, 0
	v_lshl_add_u64 v[36:37], v[36:37], 2, v[32:33]
	v_lshl_add_u64 v[38:39], v[38:39], 2, v[32:33]
	v_lshl_add_u64 v[40:41], v[40:41], 2, v[32:33]
	v_lshl_add_u64 v[42:43], v[42:43], 2, v[32:33]
	v_lshl_add_u64 v[44:45], v[44:45], 2, v[32:33]
	v_lshl_add_u64 v[46:47], v[46:47], 2, v[32:33]
	v_lshl_add_u64 v[48:49], v[48:49], 2, v[32:33]
	global_load_dword v98, v[34:35], off nt
	global_load_dword v99, v[36:37], off nt
	global_load_dword v100, v[38:39], off nt
	global_load_dword v101, v[40:41], off nt
	global_load_dword v102, v[42:43], off nt
	global_load_dword v103, v[44:45], off nt
	global_load_dword v104, v[46:47], off nt
	global_load_dword v105, v[48:49], off nt
	v_or_b32_e32 v34, 16, v50
	v_mad_i64_i32 v[34:35], s[16:17], v34, s11, 0
	v_or_b32_e32 v36, 18, v50
	v_or_b32_e32 v38, 20, v50
	v_or_b32_e32 v40, 22, v50
	v_or_b32_e32 v42, 24, v50
	v_or_b32_e32 v44, 26, v50
	v_or_b32_e32 v46, 28, v50
	v_or_b32_e32 v48, 30, v50
	v_lshl_add_u64 v[34:35], v[34:35], 2, v[32:33]
	v_mad_i64_i32 v[36:37], s[16:17], v36, s11, 0
	v_mad_i64_i32 v[38:39], s[16:17], v38, s11, 0
	v_mad_i64_i32 v[40:41], s[16:17], v40, s11, 0
	v_mad_i64_i32 v[42:43], s[16:17], v42, s11, 0
	v_mad_i64_i32 v[44:45], s[16:17], v44, s11, 0
	v_mad_i64_i32 v[46:47], s[16:17], v46, s11, 0
	v_mad_i64_i32 v[48:49], s[16:17], v48, s11, 0
	v_lshl_add_u64 v[36:37], v[36:37], 2, v[32:33]
	v_lshl_add_u64 v[38:39], v[38:39], 2, v[32:33]
	v_lshl_add_u64 v[40:41], v[40:41], 2, v[32:33]
	v_lshl_add_u64 v[42:43], v[42:43], 2, v[32:33]
	v_lshl_add_u64 v[44:45], v[44:45], 2, v[32:33]
	v_lshl_add_u64 v[46:47], v[46:47], 2, v[32:33]
	v_lshl_add_u64 v[48:49], v[48:49], 2, v[32:33]
	global_load_dword v106, v[34:35], off nt
	global_load_dword v107, v[36:37], off nt
	global_load_dword v108, v[38:39], off nt
	global_load_dword v109, v[40:41], off nt
	global_load_dword v110, v[42:43], off nt
	global_load_dword v111, v[44:45], off nt
	global_load_dword v112, v[46:47], off nt
	global_load_dword v113, v[48:49], off nt
	v_or_b32_e32 v34, 32, v50
	v_mad_i64_i32 v[34:35], s[16:17], v34, s11, 0
	v_or_b32_e32 v36, 34, v50
	v_or_b32_e32 v38, 36, v50
	v_or_b32_e32 v40, 38, v50
	v_or_b32_e32 v42, 40, v50
	v_or_b32_e32 v44, 42, v50
	v_or_b32_e32 v46, 44, v50
	v_or_b32_e32 v48, 46, v50
	v_lshl_add_u64 v[34:35], v[34:35], 2, v[32:33]
	v_mad_i64_i32 v[36:37], s[16:17], v36, s11, 0
	v_mad_i64_i32 v[38:39], s[16:17], v38, s11, 0
	v_mad_i64_i32 v[40:41], s[16:17], v40, s11, 0
	v_mad_i64_i32 v[42:43], s[16:17], v42, s11, 0
	v_mad_i64_i32 v[44:45], s[16:17], v44, s11, 0
	v_mad_i64_i32 v[46:47], s[16:17], v46, s11, 0
	v_mad_i64_i32 v[48:49], s[16:17], v48, s11, 0
	v_lshl_add_u64 v[36:37], v[36:37], 2, v[32:33]
	v_lshl_add_u64 v[38:39], v[38:39], 2, v[32:33]
	v_lshl_add_u64 v[40:41], v[40:41], 2, v[32:33]
	v_lshl_add_u64 v[42:43], v[42:43], 2, v[32:33]
	v_lshl_add_u64 v[44:45], v[44:45], 2, v[32:33]
	v_lshl_add_u64 v[46:47], v[46:47], 2, v[32:33]
	v_lshl_add_u64 v[48:49], v[48:49], 2, v[32:33]
	global_load_dword v114, v[34:35], off nt
	global_load_dword v115, v[36:37], off nt
	global_load_dword v116, v[38:39], off nt
	global_load_dword v117, v[40:41], off nt
	global_load_dword v118, v[42:43], off nt
	global_load_dword v119, v[44:45], off nt
	global_load_dword v120, v[46:47], off nt
	global_load_dword v121, v[48:49], off nt
	v_or_b32_e32 v34, 48, v50
	v_mad_i64_i32 v[34:35], s[16:17], v34, s11, 0
	v_or_b32_e32 v36, 50, v50
	v_or_b32_e32 v38, 52, v50
	v_or_b32_e32 v40, 54, v50
	v_or_b32_e32 v42, 56, v50
	v_or_b32_e32 v44, 58, v50
	v_or_b32_e32 v46, 60, v50
	v_or_b32_e32 v48, 62, v50
	v_lshl_add_u64 v[34:35], v[34:35], 2, v[32:33]
	v_mad_i64_i32 v[36:37], s[16:17], v36, s11, 0
	v_mad_i64_i32 v[38:39], s[16:17], v38, s11, 0
	v_mad_i64_i32 v[40:41], s[16:17], v40, s11, 0
	v_mad_i64_i32 v[42:43], s[16:17], v42, s11, 0
	v_mad_i64_i32 v[44:45], s[16:17], v44, s11, 0
	v_mad_i64_i32 v[46:47], s[16:17], v46, s11, 0
	v_mad_i64_i32 v[48:49], s[16:17], v48, s11, 0
	v_lshl_add_u64 v[36:37], v[36:37], 2, v[32:33]
	v_lshl_add_u64 v[38:39], v[38:39], 2, v[32:33]
	v_lshl_add_u64 v[40:41], v[40:41], 2, v[32:33]
	v_lshl_add_u64 v[42:43], v[42:43], 2, v[32:33]
	v_lshl_add_u64 v[44:45], v[44:45], 2, v[32:33]
	v_lshl_add_u64 v[46:47], v[46:47], 2, v[32:33]
	v_lshl_add_u64 v[32:33], v[48:49], 2, v[32:33]
	global_load_dword v122, v[34:35], off nt
	global_load_dword v123, v[36:37], off nt
	global_load_dword v124, v[38:39], off nt
	global_load_dword v125, v[40:41], off nt
	global_load_dword v126, v[42:43], off nt
	global_load_dword v127, v[44:45], off nt
	global_load_dword v128, v[46:47], off nt
	global_load_dword v129, v[32:33], off nt
	s_mov_b64 s[16:17], -1
	s_and_b64 vcc, exec, s[14:15]
	v_or_b32_e32 v131, s12, v86
	v_or_b32_e32 v130, s12, v90
	v_add_u32_e32 v32, 0x200, v88
	v_add_u32_e32 v33, 0x400, v88
	v_add_u32_e32 v34, 0x600, v88
	v_add_u32_e32 v35, 0x800, v88
	v_add_u32_e32 v36, 0xa00, v88
	v_add_u32_e32 v37, 0xc00, v88
	v_add_u32_e32 v38, 0xe00, v88
	v_add_u32_e32 v39, 0x1000, v88
	v_add_u32_e32 v40, 0x1200, v88
	v_add_u32_e32 v41, 0x1400, v88
	v_add_u32_e32 v42, 0x1600, v88
	v_add_u32_e32 v43, 0x1800, v88
	v_add_u32_e32 v44, 0x1a00, v88
	v_add_u32_e32 v45, 0x1c00, v88
	v_add_u32_e32 v132, 0x400, v89
	s_cbranch_vccz .LBB0_47
	s_waitcnt vmcnt(62)
	v_mul_f32_e32 v46, 0x42800000, v1
	s_waitcnt vmcnt(61)
	v_mul_f32_e32 v47, 0x42800000, v2
	ds_write2_b32 v88, v46, v47 offset0:66 offset1:132
	s_waitcnt vmcnt(60)
	v_mul_f32_e32 v46, 0x42800000, v3
	s_waitcnt vmcnt(59)
	v_mul_f32_e32 v47, 0x42800000, v4
	ds_write2_b32 v32, v46, v47 offset0:70 offset1:136
	s_waitcnt vmcnt(58)
	v_mul_f32_e32 v46, 0x42800000, v5
	s_waitcnt vmcnt(57)
	v_mul_f32_e32 v47, 0x42800000, v6
	ds_write2_b32 v33, v46, v47 offset0:74 offset1:140
	s_waitcnt vmcnt(56)
	v_mul_f32_e32 v46, 0x42800000, v7
	s_waitcnt vmcnt(55)
	v_mul_f32_e32 v47, 0x42800000, v8
	ds_write2_b32 v34, v46, v47 offset0:78 offset1:144
	s_waitcnt vmcnt(54)
	v_mul_f32_e32 v46, 0x42800000, v9
	s_waitcnt vmcnt(53)
	v_mul_f32_e32 v47, 0x42800000, v10
	ds_write2_b32 v35, v46, v47 offset0:82 offset1:148
	s_waitcnt vmcnt(52)
	v_mul_f32_e32 v46, 0x42800000, v11
	s_waitcnt vmcnt(51)
	v_mul_f32_e32 v47, 0x42800000, v12
	ds_write2_b32 v36, v46, v47 offset0:86 offset1:152
	s_waitcnt vmcnt(50)
	v_mul_f32_e32 v46, 0x42800000, v13
	s_waitcnt vmcnt(49)
	v_mul_f32_e32 v47, 0x42800000, v14
	ds_write2_b32 v37, v46, v47 offset0:90 offset1:156
	s_waitcnt vmcnt(48)
	v_mul_f32_e32 v46, 0x42800000, v15
	s_waitcnt vmcnt(47)
	v_mul_f32_e32 v47, 0x42800000, v16
	ds_write2_b32 v38, v46, v47 offset0:94 offset1:160
	s_waitcnt vmcnt(46)
	v_mul_f32_e32 v46, 0x42800000, v17
	s_waitcnt vmcnt(45)
	v_mul_f32_e32 v47, 0x42800000, v18
	ds_write2_b32 v39, v46, v47 offset0:98 offset1:164
	s_waitcnt vmcnt(44)
	v_mul_f32_e32 v46, 0x42800000, v19
	s_waitcnt vmcnt(43)
	v_mul_f32_e32 v47, 0x42800000, v20
	ds_write2_b32 v40, v46, v47 offset0:102 offset1:168
	s_waitcnt vmcnt(42)
	v_mul_f32_e32 v46, 0x42800000, v21
	s_waitcnt vmcnt(41)
	v_mul_f32_e32 v47, 0x42800000, v22
	ds_write2_b32 v41, v46, v47 offset0:106 offset1:172
	s_waitcnt vmcnt(40)
	v_mul_f32_e32 v46, 0x42800000, v23
	s_waitcnt vmcnt(39)
	v_mul_f32_e32 v47, 0x42800000, v24
	ds_write2_b32 v42, v46, v47 offset0:110 offset1:176
	s_waitcnt vmcnt(38)
	v_mul_f32_e32 v46, 0x42800000, v25
	s_waitcnt vmcnt(37)
	v_mul_f32_e32 v47, 0x42800000, v26
	ds_write2_b32 v43, v46, v47 offset0:114 offset1:180
	s_waitcnt vmcnt(36)
	v_mul_f32_e32 v46, 0x42800000, v27
	s_waitcnt vmcnt(35)
	v_mul_f32_e32 v47, 0x42800000, v28
	ds_write2_b32 v44, v46, v47 offset0:118 offset1:184
	s_waitcnt vmcnt(34)
	v_mul_f32_e32 v46, 0x42800000, v29
	s_waitcnt vmcnt(33)
	v_mul_f32_e32 v47, 0x42800000, v30
	ds_write2_b32 v45, v46, v47 offset0:122 offset1:188
	v_mul_f32_e32 v46, 0x42800000, v0
	ds_write_b32 v87, v46
	s_waitcnt vmcnt(32)
	v_mul_f32_e32 v46, 0x42800000, v31
	ds_write_b32 v88, v46 offset:8184
	s_waitcnt lgkmcnt(0)
	ds_read2_b32 v[50:51], v89 offset1:16
	ds_read2_b32 v[52:53], v89 offset0:33 offset1:49
	ds_read2_b32 v[54:55], v89 offset0:66 offset1:82
	ds_read2_b32 v[56:57], v89 offset0:99 offset1:115
	ds_read2_b32 v[58:59], v89 offset0:132 offset1:148
	ds_read2_b32 v[60:61], v89 offset0:165 offset1:181
	ds_read2_b32 v[62:63], v89 offset0:198 offset1:214
	ds_read2_b32 v[134:135], v89 offset0:231 offset1:247
	ds_read2_b32 v[136:137], v132 offset0:8 offset1:24
	ds_read2_b32 v[138:139], v132 offset0:41 offset1:57
	ds_read2_b32 v[140:141], v132 offset0:74 offset1:90
	ds_read2_b32 v[142:143], v132 offset0:107 offset1:123
	ds_read2_b32 v[144:145], v132 offset0:140 offset1:156
	ds_read2_b32 v[146:147], v132 offset0:173 offset1:189
	v_mov_b32_e32 v46, v75
	v_mov_b32_e32 v47, v75
	v_mov_b32_e32 v48, v75
	v_mov_b32_e32 v49, v75
	ds_read2_b32 v[148:149], v132 offset0:206 offset1:222
	ds_read2_b32 v[150:151], v132 offset0:239 offset1:255
	s_waitcnt lgkmcnt(0)
	v_cvt_pk_fp8_f32 v46, v50, v52
	v_cvt_pk_fp8_f32 v47, v58, v60
	v_cvt_pk_fp8_f32 v48, v136, v138
	v_cvt_pk_fp8_f32 v49, v144, v146
	s_ashr_i32 s11, s10, 31
	v_cvt_pk_fp8_f32 v46, v54, v56 op_sel:[0,0,1]
	v_cvt_pk_fp8_f32 v47, v62, v134 op_sel:[0,0,1]
	v_cvt_pk_fp8_f32 v48, v140, v142 op_sel:[0,0,1]
	v_cvt_pk_fp8_f32 v49, v148, v150 op_sel:[0,0,1]
	v_lshl_add_u64 v[152:153], v[84:85], 0, s[10:11]
	v_lshl_add_u64 v[152:153], v[152:153], 0, v[80:81]
	v_mad_i64_i32 v[154:155], s[16:17], s6, v131, v[152:153]
	v_mov_b32_e32 v232, v46
	v_mov_b32_e32 v233, v47
	v_mov_b32_e32 v234, v48
	v_mov_b32_e32 v235, v49
	v_mov_b32_e32 v240, v154
	v_mov_b32_e32 v241, v155
	s_nop 1
	v_mov_b32_e32 v46, v75
	v_mov_b32_e32 v47, v75
	v_mov_b32_e32 v48, v75
	v_mov_b32_e32 v49, v75
	v_cvt_pk_fp8_f32 v46, v51, v53
	v_cvt_pk_fp8_f32 v47, v59, v61
	v_cvt_pk_fp8_f32 v48, v137, v139
	v_cvt_pk_fp8_f32 v49, v145, v147
	v_cvt_pk_fp8_f32 v46, v55, v57 op_sel:[0,0,1]
	v_cvt_pk_fp8_f32 v47, v63, v135 op_sel:[0,0,1]
	v_cvt_pk_fp8_f32 v48, v141, v143 op_sel:[0,0,1]
	v_cvt_pk_fp8_f32 v49, v149, v151 op_sel:[0,0,1]
	v_mad_i64_i32 v[50:51], s[16:17], s6, v130, v[152:153]
	s_mov_b64 s[16:17], 0
	v_mov_b32_e32 v236, v46
	v_mov_b32_e32 v237, v47
	v_mov_b32_e32 v238, v48
	v_mov_b32_e32 v239, v49
	v_mov_b32_e32 v242, v50
	v_mov_b32_e32 v243, v51
	s_waitcnt lgkmcnt(0)
.LBB0_47:
	s_andn2_b64 vcc, exec, s[16:17]
	s_cbranch_vccnz .LBB0_49
	s_waitcnt vmcnt(59)
	ds_write2_b32 v32, v3, v4 offset0:70 offset1:136
	s_waitcnt vmcnt(57)
	ds_write2_b32 v33, v5, v6 offset0:74 offset1:140
	s_waitcnt vmcnt(55)
	ds_write2_b32 v34, v7, v8 offset0:78 offset1:144
	s_waitcnt vmcnt(53)
	ds_write2_b32 v35, v9, v10 offset0:82 offset1:148
	s_waitcnt vmcnt(51)
	ds_write2_b32 v36, v11, v12 offset0:86 offset1:152
	s_waitcnt vmcnt(49)
	ds_write2_b32 v37, v13, v14 offset0:90 offset1:156
	s_waitcnt vmcnt(47)
	ds_write2_b32 v38, v15, v16 offset0:94 offset1:160
	s_waitcnt vmcnt(45)
	ds_write2_b32 v39, v17, v18 offset0:98 offset1:164
	s_waitcnt vmcnt(43)
	ds_write2_b32 v40, v19, v20 offset0:102 offset1:168
	s_waitcnt vmcnt(41)
	ds_write2_b32 v41, v21, v22 offset0:106 offset1:172
	s_waitcnt vmcnt(39)
	ds_write2_b32 v42, v23, v24 offset0:110 offset1:176
	s_waitcnt vmcnt(37)
	ds_write2_b32 v43, v25, v26 offset0:114 offset1:180
	s_waitcnt vmcnt(35)
	ds_write2_b32 v44, v27, v28 offset0:118 offset1:184
	s_waitcnt vmcnt(33)
	ds_write2_b32 v45, v29, v30 offset0:122 offset1:188
	ds_write_b32 v87, v0
	ds_write2_b32 v88, v1, v2 offset0:66 offset1:132
	s_waitcnt vmcnt(32)
	ds_write_b32 v88, v31 offset:8184
	s_waitcnt lgkmcnt(0)
	ds_read2_b32 v[34:35], v92 offset0:33 offset1:66
	ds_read_b32 v32, v91
	ds_read_b32 v63, v93
	ds_read2_b32 v[36:37], v92 offset0:99 offset1:132
	ds_read2_b32 v[38:39], v92 offset0:165 offset1:198
	v_add_u32_e32 v46, 0x400, v92
	s_waitcnt lgkmcnt(0)
	v_max3_f32 v33, |v32|, 0, |v34|
	v_add_u32_e32 v54, 0x800, v92
	v_max3_f32 v40, v33, |v35|, |v36|
	v_mov_b32_e32 v33, v34
	v_mov_b32_e32 v34, v35
	v_max3_f32 v42, v40, |v37|, |v38|
	v_mov_b32_e32 v35, v36
	v_mov_b32_e32 v36, v37
	v_add_u32_e32 v37, 0x200, v92
	ds_read2_b32 v[40:41], v37 offset0:103 offset1:136
	v_mov_b32_e32 v37, v38
	v_mov_b32_e32 v38, v39
	v_add_u32_e32 v62, 0xc00, v92
	ds_read2_b32 v[134:135], v62 offset0:189 offset1:222
	s_waitcnt lgkmcnt(1)
	v_max3_f32 v44, v42, |v39|, |v40|
	ds_read2_b32 v[42:43], v46 offset0:41 offset1:74
	v_mov_b32_e32 v39, v40
	v_mov_b32_e32 v40, v41
	s_lshl_b32 s13, s7, 6
	s_and_b32 s13, s13, 0xffffff00
	s_waitcnt lgkmcnt(0)
	v_max3_f32 v47, v44, |v41|, |v42|
	ds_read2_b32 v[44:45], v46 offset0:107 offset1:140
	v_mov_b32_e32 v41, v42
	v_mov_b32_e32 v42, v43
	s_and_b32 s11, s12, 0x60
	s_add_i32 s13, s13, s23
	s_waitcnt lgkmcnt(0)
	v_max3_f32 v48, v47, |v43|, |v44|
	ds_read2_b32 v[46:47], v46 offset0:173 offset1:206
	v_mov_b32_e32 v43, v44
	v_mov_b32_e32 v44, v45
	s_or_b32 s11, s13, s11
	v_mov_b32_e32 v141, v75
	s_waitcnt lgkmcnt(0)
	v_max3_f32 v50, v48, |v45|, |v46|
	v_add_u32_e32 v45, 0x600, v92
	ds_read2_b32 v[48:49], v45 offset0:111 offset1:144
	v_mov_b32_e32 v45, v46
	v_mov_b32_e32 v46, v47
	s_waitcnt lgkmcnt(0)
	v_max3_f32 v52, v50, |v47|, |v48|
	ds_read2_b32 v[50:51], v54 offset0:49 offset1:82
	v_mov_b32_e32 v47, v48
	v_mov_b32_e32 v48, v49
	s_waitcnt lgkmcnt(0)
	v_max3_f32 v55, v52, |v49|, |v50|
	ds_read2_b32 v[52:53], v54 offset0:115 offset1:148
	v_mov_b32_e32 v49, v50
	v_mov_b32_e32 v50, v51
	s_waitcnt lgkmcnt(0)
	v_max3_f32 v56, v55, |v51|, |v52|
	ds_read2_b32 v[54:55], v54 offset0:181 offset1:214
	v_mov_b32_e32 v51, v52
	v_mov_b32_e32 v52, v53
	s_waitcnt lgkmcnt(0)
	v_max3_f32 v58, v56, |v53|, |v54|
	v_add_u32_e32 v53, 0xa00, v92
	ds_read2_b32 v[56:57], v53 offset0:119 offset1:152
	v_mov_b32_e32 v53, v54
	v_mov_b32_e32 v54, v55
	s_waitcnt lgkmcnt(0)
	v_max3_f32 v60, v58, |v55|, |v56|
	ds_read2_b32 v[58:59], v62 offset0:57 offset1:90
	v_mov_b32_e32 v55, v56
	v_mov_b32_e32 v56, v57
	s_waitcnt lgkmcnt(0)
	v_max3_f32 v133, v60, |v57|, |v58|
	ds_read2_b32 v[60:61], v62 offset0:123 offset1:156
	v_mov_b32_e32 v57, v58
	v_mov_b32_e32 v58, v59
	s_waitcnt lgkmcnt(0)
	v_max3_f32 v133, v133, |v59|, |v60|
	v_max3_f32 v62, v133, |v61|, |v134|
	v_max3_f32 v133, v62, |v135|, |v63|
	v_mov_b32_e32 v59, v60
	v_mov_b32_e32 v60, v61
	v_mov_b32_e32 v61, v134
	v_bfe_u32 v134, v133, 23, 8
	v_and_or_b32 v133, v133, s20, 0.5
	v_cmp_lt_f32_e32 vcc, s21, v133
	v_mov_b32_e32 v62, v135
	s_nop 0
	v_addc_co_u32_e32 v133, vcc, v134, v97, vcc
	v_max_i32_e32 v133, 0xffffff82, v133
	v_add_u32_e32 v140, 0x7f, v133
	v_lshlrev_b32_e32 v133, 23, v140
	v_cvt_scalef32_2xpk16_fp6_f32 v[134:139], v[32:47], v[48:63], v133
	v_or_b32_e32 v32, s10, v82
	v_or_b32_e32 v34, s11, v72
	v_ashrrev_i32_e32 v33, 31, v32
	v_mad_i64_i32 v[34:35], s[16:17], s6, v34, v[84:85]
	v_lshl_add_u64 v[32:33], v[34:35], 0, v[32:33]
	v_mov_b32_e32 v232, v134
	v_mov_b32_e32 v233, v135
	v_mov_b32_e32 v234, v136
	v_mov_b32_e32 v235, v137
	v_mov_b32_e32 v240, v32
	v_mov_b32_e32 v241, v33
	v_mov_b32_e32 v236, v138
	v_mov_b32_e32 v237, v139
	v_mov_b32_e32 v238, v140
	v_mov_b32_e32 v239, v141
	s_waitcnt lgkmcnt(0)

.LBB0_53:
	s_waitcnt vmcnt(31)
	v_mul_f32_e32 v39, 0x42800000, v98
	s_waitcnt vmcnt(30)
	v_mul_f32_e32 v40, 0x42800000, v99
	ds_write2_b32 v87, v39, v40 offset1:66
	s_waitcnt vmcnt(29)
	v_mul_f32_e32 v39, 0x42800000, v100
	s_waitcnt vmcnt(28)
	v_mul_f32_e32 v40, 0x42800000, v101
	ds_write2_b32 v87, v39, v40 offset0:132 offset1:198
	s_waitcnt vmcnt(27)
	v_mul_f32_e32 v39, 0x42800000, v102
	s_waitcnt vmcnt(26)
	v_mul_f32_e32 v40, 0x42800000, v103
	ds_write2_b32 v38, v39, v40 offset0:8 offset1:74
	s_waitcnt vmcnt(25)
	v_mul_f32_e32 v39, 0x42800000, v104
	s_waitcnt vmcnt(24)
	v_mul_f32_e32 v40, 0x42800000, v105
	ds_write2_b32 v38, v39, v40 offset0:140 offset1:206
	s_waitcnt vmcnt(23)
	v_mul_f32_e32 v39, 0x42800000, v106
	s_waitcnt vmcnt(22)
	v_mul_f32_e32 v40, 0x42800000, v107
	ds_write2_b32 v37, v39, v40 offset0:16 offset1:82
	s_waitcnt vmcnt(21)
	v_mul_f32_e32 v39, 0x42800000, v108
	s_waitcnt vmcnt(20)
	v_mul_f32_e32 v40, 0x42800000, v109
	ds_write2_b32 v37, v39, v40 offset0:148 offset1:214
	s_waitcnt vmcnt(19)
	v_mul_f32_e32 v39, 0x42800000, v110
	s_waitcnt vmcnt(18)
	v_mul_f32_e32 v40, 0x42800000, v111
	ds_write2_b32 v36, v39, v40 offset0:24 offset1:90
	s_waitcnt vmcnt(17)
	v_mul_f32_e32 v39, 0x42800000, v112
	s_waitcnt vmcnt(16)
	v_mul_f32_e32 v40, 0x42800000, v113
	ds_write2_b32 v36, v39, v40 offset0:156 offset1:222
	s_waitcnt vmcnt(15)
	v_mul_f32_e32 v39, 0x42800000, v114
	s_waitcnt vmcnt(14)
	v_mul_f32_e32 v40, 0x42800000, v115
	ds_write2_b32 v35, v39, v40 offset0:32 offset1:98
	s_waitcnt vmcnt(13)
	v_mul_f32_e32 v39, 0x42800000, v116
	s_waitcnt vmcnt(12)
	v_mul_f32_e32 v40, 0x42800000, v117
	ds_write2_b32 v35, v39, v40 offset0:164 offset1:230
	s_waitcnt vmcnt(11)
	v_mul_f32_e32 v39, 0x42800000, v118
	s_waitcnt vmcnt(10)
	v_mul_f32_e32 v40, 0x42800000, v119
	ds_write2_b32 v34, v39, v40 offset0:40 offset1:106
	s_waitcnt vmcnt(9)
	v_mul_f32_e32 v39, 0x42800000, v120
	s_waitcnt vmcnt(8)
	v_mul_f32_e32 v40, 0x42800000, v121
	ds_write2_b32 v34, v39, v40 offset0:172 offset1:238
	s_waitcnt vmcnt(7)
	v_mul_f32_e32 v39, 0x42800000, v122
	s_waitcnt vmcnt(6)
	v_mul_f32_e32 v40, 0x42800000, v123
	ds_write2_b32 v33, v39, v40 offset0:48 offset1:114
	s_waitcnt vmcnt(5)
	v_mul_f32_e32 v39, 0x42800000, v124
	s_waitcnt vmcnt(4)
	v_mul_f32_e32 v40, 0x42800000, v125
	ds_write2_b32 v33, v39, v40 offset0:180 offset1:246
	s_waitcnt vmcnt(3)
	v_mul_f32_e32 v39, 0x42800000, v126
	s_waitcnt vmcnt(2)
	v_mul_f32_e32 v40, 0x42800000, v127
	ds_write2_b32 v32, v39, v40 offset0:56 offset1:122
	s_waitcnt vmcnt(1)
	v_mul_f32_e32 v39, 0x42800000, v128
	s_waitcnt vmcnt(0)
	v_mul_f32_e32 v40, 0x42800000, v129
	ds_write2_b32 v32, v39, v40 offset0:188 offset1:254
	s_waitcnt lgkmcnt(0)
	ds_read2_b32 v[44:45], v89 offset1:16
	ds_read2_b32 v[46:47], v89 offset0:33 offset1:49
	ds_read2_b32 v[50:51], v89 offset0:66 offset1:82
	ds_read2_b32 v[52:53], v89 offset0:99 offset1:115
	ds_read2_b32 v[54:55], v89 offset0:132 offset1:148
	ds_read2_b32 v[56:57], v89 offset0:165 offset1:181
	ds_read2_b32 v[58:59], v89 offset0:198 offset1:214
	ds_read2_b32 v[60:61], v89 offset0:231 offset1:247
	ds_read2_b32 v[62:63], v132 offset0:8 offset1:24
	ds_read2_b32 v[134:135], v132 offset0:41 offset1:57
	ds_read2_b32 v[136:137], v132 offset0:74 offset1:90
	ds_read2_b32 v[138:139], v132 offset0:107 offset1:123
	ds_read2_b32 v[140:141], v132 offset0:140 offset1:156
	ds_read2_b32 v[142:143], v132 offset0:173 offset1:189
	s_ashr_i32 s11, s10, 31
	v_lshl_add_u64 v[40:41], v[84:85], 0, s[10:11]
	v_lshl_add_u64 v[48:49], v[40:41], 0, v[80:81]
	v_mov_b32_e32 v40, v75
	s_waitcnt lgkmcnt(0)
	v_cvt_pk_fp8_f32 v40, v44, v46
	v_mov_b32_e32 v41, v75
	v_mov_b32_e32 v42, v75
	ds_read2_b32 v[144:145], v132 offset0:206 offset1:222
	ds_read2_b32 v[132:133], v132 offset0:239 offset1:255
	v_mov_b32_e32 v43, v75
	v_mov_b32_e32 v44, v75
	v_cvt_pk_fp8_f32 v41, v54, v56
	v_cvt_pk_fp8_f32 v42, v62, v134
	v_cvt_pk_fp8_f32 v43, v140, v142
	v_cvt_pk_fp8_f32 v44, v45, v47
	v_mov_b32_e32 v45, v75
	v_mov_b32_e32 v46, v75
	v_mov_b32_e32 v47, v75
	v_cvt_pk_fp8_f32 v45, v55, v57
	v_cvt_pk_fp8_f32 v46, v63, v135
	v_cvt_pk_fp8_f32 v47, v141, v143
	v_cvt_pk_fp8_f32 v40, v50, v52 op_sel:[0,0,1]
	v_cvt_pk_fp8_f32 v41, v58, v60 op_sel:[0,0,1]
	v_cvt_pk_fp8_f32 v42, v136, v138 op_sel:[0,0,1]
	s_waitcnt lgkmcnt(0)
	v_cvt_pk_fp8_f32 v43, v144, v132 op_sel:[0,0,1]
	v_cvt_pk_fp8_f32 v44, v51, v53 op_sel:[0,0,1]
	v_cvt_pk_fp8_f32 v45, v59, v61 op_sel:[0,0,1]
	v_cvt_pk_fp8_f32 v46, v137, v139 op_sel:[0,0,1]
	v_cvt_pk_fp8_f32 v47, v145, v133 op_sel:[0,0,1]
	v_mad_i64_i32 v[146:147], s[14:15], s6, v131, v[48:49]
	global_store_dwordx4 v[240:241], v[232:235], off
	global_store_dwordx4 v[146:147], v[40:43], off offset:64
	s_nop 1
	v_mad_i64_i32 v[40:41], s[14:15], s6, v130, v[48:49]
	global_store_dwordx4 v[242:243], v[236:239], off
	global_store_dwordx4 v[40:41], v[44:47], off offset:64
	s_waitcnt lgkmcnt(0)
	s_cbranch_execnz .LBB0_39
.LBB0_54:
	s_waitcnt vmcnt(30)
	ds_write2_b32 v87, v98, v99 offset1:66
	s_waitcnt vmcnt(28)
	ds_write2_b32 v87, v100, v101 offset0:132 offset1:198
	s_waitcnt vmcnt(26)
	ds_write2_b32 v38, v102, v103 offset0:8 offset1:74
	s_waitcnt vmcnt(24)
	ds_write2_b32 v38, v104, v105 offset0:140 offset1:206
	s_waitcnt vmcnt(22)
	ds_write2_b32 v37, v106, v107 offset0:16 offset1:82
	s_waitcnt vmcnt(20)
	ds_write2_b32 v37, v108, v109 offset0:148 offset1:214
	s_waitcnt vmcnt(18)
	ds_write2_b32 v36, v110, v111 offset0:24 offset1:90
	s_waitcnt vmcnt(16)
	ds_write2_b32 v36, v112, v113 offset0:156 offset1:222
	s_waitcnt vmcnt(14)
	ds_write2_b32 v35, v114, v115 offset0:32 offset1:98
	s_waitcnt vmcnt(12)
	ds_write2_b32 v35, v116, v117 offset0:164 offset1:230
	s_waitcnt vmcnt(10)
	ds_write2_b32 v34, v118, v119 offset0:40 offset1:106
	s_waitcnt vmcnt(8)
	ds_write2_b32 v34, v120, v121 offset0:172 offset1:238
	s_waitcnt vmcnt(6)
	ds_write2_b32 v33, v122, v123 offset0:48 offset1:114
	s_waitcnt vmcnt(4)
	ds_write2_b32 v33, v124, v125 offset0:180 offset1:246
	s_waitcnt vmcnt(2)
	ds_write2_b32 v32, v126, v127 offset0:56 offset1:122
	s_waitcnt vmcnt(0)
	ds_write2_b32 v32, v128, v129 offset0:188 offset1:254
	s_waitcnt lgkmcnt(0)
	ds_read2_b32 v[32:33], v91 offset1:33
	ds_read2_b32 v[34:35], v91 offset0:66 offset1:99
	ds_read2_b32 v[36:37], v91 offset0:132 offset1:165
	ds_read2_b32 v[38:39], v91 offset0:198 offset1:231
	v_add_u32_e32 v46, 0x400, v91
	s_waitcnt lgkmcnt(0)
	v_max3_f32 v98, |v32|, 0, |v33|
	v_max3_f32 v98, v98, |v34|, |v35|
	ds_read2_b32 v[40:41], v46 offset0:8 offset1:41
	ds_read2_b32 v[42:43], v46 offset0:74 offset1:107
	ds_read2_b32 v[44:45], v46 offset0:140 offset1:173
	ds_read2_b32 v[46:47], v46 offset0:206 offset1:239
	v_max3_f32 v98, v98, |v36|, |v37|
	v_max3_f32 v98, v98, |v38|, |v39|
	s_waitcnt lgkmcnt(3)
	v_max3_f32 v98, v98, |v40|, |v41|
	v_add_u32_e32 v54, 0x800, v91
	s_waitcnt lgkmcnt(2)
	v_max3_f32 v98, v98, |v42|, |v43|
	ds_read2_b32 v[48:49], v54 offset0:16 offset1:49
	ds_read2_b32 v[50:51], v54 offset0:82 offset1:115
	ds_read2_b32 v[52:53], v54 offset0:148 offset1:181
	ds_read2_b32 v[54:55], v54 offset0:214 offset1:247
	s_waitcnt lgkmcnt(5)
	v_max3_f32 v98, v98, |v44|, |v45|
	s_waitcnt lgkmcnt(4)
	v_max3_f32 v98, v98, |v46|, |v47|
	s_waitcnt lgkmcnt(3)
	v_max3_f32 v98, v98, |v48|, |v49|
	v_add_u32_e32 v60, 0xc00, v91
	s_waitcnt lgkmcnt(2)
	v_max3_f32 v98, v98, |v50|, |v51|
	ds_read2_b32 v[56:57], v60 offset0:24 offset1:57
	ds_read2_b32 v[58:59], v60 offset0:90 offset1:123
	ds_read2_b32 v[60:61], v60 offset0:156 offset1:189
	ds_read_b32 v62, v91 offset:3960
	ds_read_b32 v63, v93
	s_waitcnt lgkmcnt(6)
	v_max3_f32 v98, v98, |v52|, |v53|
	s_waitcnt lgkmcnt(5)
	v_max3_f32 v98, v98, |v54|, |v55|
	s_waitcnt lgkmcnt(4)
	v_max3_f32 v98, v98, |v56|, |v57|
	s_waitcnt lgkmcnt(3)
	v_max3_f32 v98, v98, |v58|, |v59|
	s_waitcnt lgkmcnt(2)
	v_max3_f32 v98, v98, |v60|, |v61|
	s_waitcnt lgkmcnt(0)
	v_max3_f32 v98, v98, |v62|, |v63|
	v_bfe_u32 v99, v98, 23, 8
	v_and_or_b32 v98, v98, s20, 0.5
	v_cmp_lt_f32_e32 vcc, s21, v98
	s_lshl_b32 s7, s7, 6
	s_and_b32 s7, s7, 0xffffff00
	v_addc_co_u32_e32 v98, vcc, v99, v97, vcc
	v_max_i32_e32 v98, 0xffffff82, v98
	s_and_b32 s11, s12, 0x60
	s_add_i32 s7, s7, s23
	v_add_u32_e32 v104, 0x7f, v98
	s_or_b32 s7, s7, s11
	v_lshlrev_b32_e32 v105, 23, v104
	v_cvt_scalef32_2xpk16_fp6_f32 v[98:103], v[32:47], v[48:63], v105
	v_or_b32_e32 v32, s7, v72
	s_ashr_i32 s11, s10, 31
	v_mad_i64_i32 v[32:33], s[6:7], s6, v32, v[84:85]
	v_lshl_add_u64 v[34:35], s[10:11], 0, v[82:83]
	v_lshl_add_u64 v[32:33], v[32:33], 0, v[34:35]
	v_mov_b32_e32 v105, v75
	global_store_dwordx4 v[240:241], v[232:235], off
	global_store_dwordx4 v[32:33], v[98:101], off offset:32
	global_store_dwordx4 v[240:241], v[236:239], off offset:64
	global_store_dwordx4 v[32:33], v[102:105], off offset:96
	s_waitcnt lgkmcnt(0)
	s_branch .LBB0_39
